# adds: gate/up K-loop stages one A half-tile one load segment later (4+4 instead of 6+2 LDS-DMA per segment pair)
# baseline (speedup 1.0000x reference)
; #define PG8_GREAD(dst, u, par) do { _Pragma("unroll") for (int h_ = 0; h_ < 2; ++h_) _Pragma("unroll") for (int i_ = 0; i_ < 2; ++i_) { const int rl_ = 128 * h_ + grl[i_]; \
;         const int tk_ = *(const PG8_LAS int*)(gtab + (par) * 2048 + rl_ * 8); const unsigned tok_ = (rl_ < (u).rows) ? ((unsigned)tk_ >> 2) : 0u; dst[h_][i_] = tok_ * (unsigned)(K * 2) + gcb[i_]; } } while (0)
; #define PG8_STAGE(bufoff, gbase, voff) do { _Pragma("unroll") for (int _i = 0; _i < 2; ++_i) \
;         __builtin_amdgcn_global_load_lds((const unsigned*)((const char*)(gbase) + (voff)[_i]), (PG8_LAS unsigned*)(lds + (bufoff) + ldsw + _i * 8192), 16, 0, 0); } while (0)
; #define PG8_WAIT_V(n) asm volatile("s_waitcnt vmcnt(" #n ")" ::: "memory")
; template <class Epi, class Sched, bool ALIGN_EPI = false, bool SP2 = false, bool GATHER = false>
; __device__ __forceinline__ void gemm_phase(PG8_LAS unsigned char* lds, const Gemm g, const Sched& S, const Epi& E, const int2* gslot = nullptr, PG8_LAS unsigned char* gtab = nullptr) {
;     ...
;             const char* a1 = cA + (size_t)(t + 1) * kstep;
;             const char* a2 = last ? nA : cA + (size_t)(t + 2) * kstep; const char* b2 = last ? nB : cB + (size_t)(t + 2) * kstep;
;             const char* a3 = a2 + kstep; const char* b3 = b2 + kstep;
;             if (last && has_next) S.a_ready(nxt);
;             if constexpr (GATHER) { if (last) { if (has_next) { PG8_GREAD(vN, nxt, (ui + 1) & 1); } else { _Pragma("unroll") for (int h_ = 0; h_ < 2; ++h_) _Pragma("unroll") for (int i_ = 0; i_ < 2; ++i_) vN[h_][i_] = vC[h_][i_]; } } }
;             unsigned vS[2][2];
; #pragma unroll
;             for (int h_ = 0; h_ < 2; ++h_)
; #pragma unroll
;                 for (int i_ = 0; i_ < 2; ++i_) vS[h_][i_] = (GATHER && last) ? vN[h_][i_] : vC[h_][i_];
;             if constexpr (SP2) {
;             PG8_LDB(B0, 0, 0); PG8_LDB(B1, 0, 1); PG8_SCHED; PG8_LDA(At, 0, 0); PG8_STAGE(PG8_SA(1, 1), a1 + PG8_AH(1), PG8_VA(vC, 1));
;             PG8_WAIT_V(8); PG8_WAIT_L(0); PG8_BAR; PG8_MMA(0, 0, At, B0); PG8_MMA(0, 1, At, B1); PG8_BAR; PG8_SCHED;
;             PG8_LDA(At, 0, 1); PG8_STAGE(PG8_SB(0, 0), b2, voffB); PG8_STAGE(PG8_SB(0, 1), b2 + hstep, voffB); PG8_STAGE(PG8_SA(0, 0), a2, PG8_VA(vS, 0));
;             PG8_WAIT_V(8); PG8_WAIT_L(0); PG8_BAR; PG8_MMA(1, 0, At, B0); PG8_MMA(1, 1, At, B1); PG8_BAR; PG8_SCHED;
.LBB0_1093:
	s_add_u32 s70, s18, s60
	s_addc_u32 s71, s19, s61
	s_add_u32 vcc_lo, s70, 0x34000100
	s_addc_u32 vcc_hi, s71, 0
	s_and_b64 s[70:71], s[72:73], exec
	s_cselect_b32 s71, s25, vcc_hi
	s_cselect_b32 s70, s24, vcc_lo
	s_add_u32 vcc_lo, s21, s60
	s_addc_u32 vcc_hi, s37, s61
	s_and_b64 s[72:73], s[72:73], exec
	s_cselect_b32 vcc_hi, s53, vcc_hi
	s_cselect_b32 vcc_lo, s52, vcc_lo
	s_add_i32 s72, 0, 0x10000
	v_add_u32_e32 v139, s72, v155
	s_add_i32 s2, 0, 0x14000
	ds_read_b128 v[140:143], v139
	ds_read_b128 v[162:165], v139 offset:1024
	ds_read_b128 v[180:183], v139 offset:2048
	ds_read_b128 v[188:191], v139 offset:3072
	v_add_u32_e32 v139, s2, v155
	ds_read_b128 v[192:195], v139
	ds_read_b128 v[196:199], v139 offset:1024
	ds_read_b128 v[200:203], v139 offset:2048
	ds_read_b128 v[204:207], v139 offset:3072
	v_lshl_add_u64 v[144:145], v[132:133], 0, s[60:61]
	s_add_i32 m0, s97, 0xc000
	ds_read_b128 v[208:211], v184
	ds_read_b128 v[212:215], v184 offset:1024
	ds_read_b128 v[216:219], v184 offset:2048
	ds_read_b128 v[220:223], v184 offset:3072
	ds_read_b128 v[224:227], v184 offset:4096
	ds_read_b128 v[230:233], v184 offset:5120
	ds_read_b128 v[236:239], v184 offset:6144
	ds_read_b128 v[240:243], v184 offset:7168
	global_load_lds_dwordx4 v[144:145], off
	v_lshl_add_u64 v[144:145], v[130:131], 0, s[60:61]
	s_add_i32 m0, s97, 0xe000
	s_nop 0
	global_load_lds_dwordx4 v[144:145], off
	s_waitcnt vmcnt(8)
	s_waitcnt lgkmcnt(0)
	s_barrier
	s_setprio 1
	s_waitcnt lgkmcnt(0)
	v_mfma_f32_16x16x32_bf16 v[122:125], v[140:143], v[208:211], v[122:125]
	v_mfma_f32_16x16x32_bf16 v[114:117], v[180:183], v[208:211], v[114:117]
	v_mfma_f32_16x16x32_bf16 v[106:109], v[140:143], v[216:219], v[106:109]
	v_mfma_f32_16x16x32_bf16 v[98:101], v[180:183], v[216:219], v[98:101]
	v_mfma_f32_16x16x32_bf16 v[94:97], v[140:143], v[224:227], v[94:97]
	v_mfma_f32_16x16x32_bf16 v[90:93], v[180:183], v[224:227], v[90:93]
	v_mfma_f32_16x16x32_bf16 v[86:89], v[140:143], v[236:239], v[86:89]
	v_mfma_f32_16x16x32_bf16 v[82:85], v[180:183], v[236:239], v[82:85]
	v_mfma_f32_16x16x32_bf16 v[122:125], v[162:165], v[212:215], v[122:125]
	v_mfma_f32_16x16x32_bf16 v[114:117], v[188:191], v[212:215], v[114:117]
	v_mfma_f32_16x16x32_bf16 v[106:109], v[162:165], v[220:223], v[106:109]
	v_mfma_f32_16x16x32_bf16 v[98:101], v[188:191], v[220:223], v[98:101]
	v_mfma_f32_16x16x32_bf16 v[94:97], v[162:165], v[230:233], v[94:97]
	v_mfma_f32_16x16x32_bf16 v[90:93], v[188:191], v[230:233], v[90:93]
	v_mfma_f32_16x16x32_bf16 v[86:89], v[162:165], v[240:243], v[86:89]
	v_mfma_f32_16x16x32_bf16 v[82:85], v[188:191], v[240:243], v[82:85]
	s_setprio 0
	s_setprio 1
	v_mfma_f32_16x16x32_bf16 v[78:81], v[192:195], v[208:211], v[78:81]
	v_mfma_f32_16x16x32_bf16 v[74:77], v[200:203], v[208:211], v[74:77]
	v_mfma_f32_16x16x32_bf16 v[70:73], v[192:195], v[216:219], v[70:73]
	v_mfma_f32_16x16x32_bf16 v[66:69], v[200:203], v[216:219], v[66:69]
	v_mfma_f32_16x16x32_bf16 v[62:65], v[192:195], v[224:227], v[62:65]
	v_mfma_f32_16x16x32_bf16 v[58:61], v[200:203], v[224:227], v[58:61]
	v_mfma_f32_16x16x32_bf16 v[54:57], v[192:195], v[236:239], v[54:57]
	v_mfma_f32_16x16x32_bf16 v[50:53], v[200:203], v[236:239], v[50:53]
	v_mfma_f32_16x16x32_bf16 v[78:81], v[196:199], v[212:215], v[78:81]
	v_mfma_f32_16x16x32_bf16 v[74:77], v[204:207], v[212:215], v[74:77]
	v_mfma_f32_16x16x32_bf16 v[70:73], v[196:199], v[220:223], v[70:73]
	v_mfma_f32_16x16x32_bf16 v[66:69], v[204:207], v[220:223], v[66:69]
	v_mfma_f32_16x16x32_bf16 v[62:65], v[196:199], v[230:233], v[62:65]
	v_mfma_f32_16x16x32_bf16 v[58:61], v[204:207], v[230:233], v[58:61]
	v_mfma_f32_16x16x32_bf16 v[54:57], v[196:199], v[240:243], v[54:57]
	v_mfma_f32_16x16x32_bf16 v[50:53], v[204:207], v[240:243], v[50:53]
	s_setprio 0
	s_barrier
	s_add_i32 s72, s72, s47
	v_lshl_add_u64 v[166:167], vcc, 0, v[148:149]
	s_mov_b32 m0, s72
	ds_read_b128 v[208:211], v184 offset:16384
	ds_read_b128 v[212:215], v184 offset:17408
	ds_read_b128 v[216:219], v184 offset:18432
	ds_read_b128 v[220:223], v184 offset:19456
	ds_read_b128 v[224:227], v184 offset:20480
	ds_read_b128 v[230:233], v184 offset:21504
	ds_read_b128 v[236:239], v184 offset:22528
	ds_read_b128 v[240:243], v184 offset:23552
	global_load_lds_dwordx4 v[166:167], off
	s_add_i32 m0, s72, 0x2000
	s_add_u32 s72, vcc_lo, 0x40000
	v_lshl_add_u64 v[244:245], vcc, 0, v[150:151]
	s_addc_u32 s73, vcc_hi, 0
	s_add_i32 s2, s2, s47
	global_load_lds_dwordx4 v[244:245], off
	v_lshl_add_u64 v[144:145], s[72:73], 0, v[148:149]
	s_mov_b32 m0, s2
	v_mov_b32_e32 v139, v1
	global_load_lds_dwordx4 v[144:145], off
	v_lshl_add_u64 v[144:145], s[72:73], 0, v[150:151]
	s_add_i32 m0, s2, 0x2000
	v_lshl_add_u64 v[246:247], s[70:71], 0, v[0:1]
	global_load_lds_dwordx4 v[144:145], off
	v_lshl_add_u64 v[248:249], s[70:71], 0, v[138:139]
	s_waitcnt vmcnt(6)
	s_waitcnt lgkmcnt(0)
	s_barrier
; #define PG8_STAGE(bufoff, gbase, voff) do { _Pragma("unroll") for (int _i = 0; _i < 2; ++_i) \
;         __builtin_amdgcn_global_load_lds((const unsigned*)((const char*)(gbase) + (voff)[_i]), (PG8_LAS unsigned*)(lds + (bufoff) + ldsw + _i * 8192), 16, 0, 0); } while (0)
; #define PG8_LDA(dst, b, h) do { _Pragma("unroll") for (int m = 0; m < 4; ++m) _Pragma("unroll") for (int k = 0; k < 2; ++k) dst[m][k] = *(const PG8_LAS bf16x8*)(lds + PG8_SA(b, h) + aoff + m * 2048 + k * 1024); } while (0)
; #define PG8_LDB(dst, b, h) do { _Pragma("unroll") for (int n = 0; n < 2; ++n) _Pragma("unroll") for (int k = 0; k < 2; ++k) dst[n][k] = *(const PG8_LAS bf16x8*)(lds + PG8_SB(b, h) + boff + n * 2048 + k * 1024); } while (0)
; #define PG8_MMA(ai, bj, At, Bt) do { __builtin_amdgcn_s_setprio(1); _Pragma("unroll") for (int m = 0; m < 4; ++m) _Pragma("unroll") for (int n = 0; n < 2; ++n) _Pragma("unroll") for (int k = 0; k < 2; ++k) \
;         acc[ai][bj][m][n] = __builtin_amdgcn_mfma_f32_16x16x32_bf16(Bt[n][k], At[m][k], acc[ai][bj][m][n], 0, 0, 0); __builtin_amdgcn_s_setprio(0); } while (0)
; #define PG8_WAIT_V(n) asm volatile("s_waitcnt vmcnt(" #n ")" ::: "memory")
; #define PG8_WAIT_L(n) asm volatile("s_waitcnt lgkmcnt(" #n ")" ::: "memory")
; #define PG8_BAR __builtin_amdgcn_s_barrier()
; #define PG8_SCHED __builtin_amdgcn_sched_barrier(0)
; template <class Epi, class Sched, bool ALIGN_EPI = false, bool SP2 = false, bool GATHER = false>
; __device__ __forceinline__ void gemm_phase(PG8_LAS unsigned char* lds, const Gemm g, const Sched& S, const Epi& E, const int2* gslot = nullptr, PG8_LAS unsigned char* gtab = nullptr) {
;     ...
;             PG8_WAIT_V(8); PG8_WAIT_L(0); PG8_BAR; PG8_MMA(1, 0, At, B0); PG8_MMA(1, 1, At, B1); PG8_BAR; PG8_SCHED;
;             PG8_LDB(B0, 1, 0); PG8_LDB(B1, 1, 1); PG8_SCHED; PG8_LDA(At, 1, 0); PG8_STAGE(PG8_SA(0, 1), a2 + PG8_AH(1), PG8_VA(vS, 1));
;             PG8_WAIT_V(8); PG8_WAIT_L(0); PG8_BAR; PG8_MMA(0, 0, At, B0); PG8_MMA(0, 1, At, B1); PG8_BAR; PG8_SCHED;
	s_setprio 1
	s_waitcnt lgkmcnt(0)
	v_mfma_f32_16x16x32_bf16 v[46:49], v[140:143], v[208:211], v[46:49]
	v_mfma_f32_16x16x32_bf16 v[42:45], v[180:183], v[208:211], v[42:45]
	v_mfma_f32_16x16x32_bf16 v[38:41], v[140:143], v[216:219], v[38:41]
	v_mfma_f32_16x16x32_bf16 v[34:37], v[180:183], v[216:219], v[34:37]
	v_mfma_f32_16x16x32_bf16 v[30:33], v[140:143], v[224:227], v[30:33]
	v_mfma_f32_16x16x32_bf16 v[26:29], v[180:183], v[224:227], v[26:29]
	v_mfma_f32_16x16x32_bf16 v[6:9], v[140:143], v[236:239], v[6:9]
	v_mfma_f32_16x16x32_bf16 v[2:5], v[180:183], v[236:239], v[2:5]
	v_mfma_f32_16x16x32_bf16 v[46:49], v[162:165], v[212:215], v[46:49]
	v_mfma_f32_16x16x32_bf16 v[42:45], v[188:191], v[212:215], v[42:45]
	v_mfma_f32_16x16x32_bf16 v[38:41], v[162:165], v[220:223], v[38:41]
	v_mfma_f32_16x16x32_bf16 v[34:37], v[188:191], v[220:223], v[34:37]
	v_mfma_f32_16x16x32_bf16 v[30:33], v[162:165], v[230:233], v[30:33]
	v_mfma_f32_16x16x32_bf16 v[26:29], v[188:191], v[230:233], v[26:29]
	v_mfma_f32_16x16x32_bf16 v[6:9], v[162:165], v[240:243], v[6:9]
	v_mfma_f32_16x16x32_bf16 v[2:5], v[188:191], v[240:243], v[2:5]
	s_setprio 0
	s_setprio 1
	v_mfma_f32_16x16x32_bf16 v[22:25], v[192:195], v[208:211], v[22:25]
	v_mfma_f32_16x16x32_bf16 v[18:21], v[200:203], v[208:211], v[18:21]
	v_mfma_f32_16x16x32_bf16 v[14:17], v[192:195], v[216:219], v[14:17]
	v_mfma_f32_16x16x32_bf16 v[10:13], v[200:203], v[216:219], v[10:13]
	v_mfma_f32_16x16x32_bf16 v[102:105], v[192:195], v[224:227], v[102:105]
	v_mfma_f32_16x16x32_bf16 v[110:113], v[200:203], v[224:227], v[110:113]
	v_mfma_f32_16x16x32_bf16 v[118:121], v[192:195], v[236:239], v[118:121]
	v_mfma_f32_16x16x32_bf16 v[126:129], v[200:203], v[236:239], v[126:129]
	v_mfma_f32_16x16x32_bf16 v[22:25], v[196:199], v[212:215], v[22:25]
	v_mfma_f32_16x16x32_bf16 v[18:21], v[204:207], v[212:215], v[18:21]
	v_mfma_f32_16x16x32_bf16 v[14:17], v[196:199], v[220:223], v[14:17]
	v_mfma_f32_16x16x32_bf16 v[10:13], v[204:207], v[220:223], v[10:13]
	v_mfma_f32_16x16x32_bf16 v[102:105], v[196:199], v[230:233], v[102:105]
	v_mfma_f32_16x16x32_bf16 v[110:113], v[204:207], v[230:233], v[110:113]
	v_mfma_f32_16x16x32_bf16 v[118:121], v[196:199], v[240:243], v[118:121]
	v_mfma_f32_16x16x32_bf16 v[126:129], v[204:207], v[240:243], v[126:129]
	s_setprio 0
	s_barrier
	s_mov_b32 m0, s97
	s_nop 0
	global_load_lds_dwordx4 v0, s[70:71]
	s_mov_b32 m0, s66
	s_nop 0
	global_load_lds_dwordx4 v138, s[70:71]
	s_add_i32 s2, 0, 0x18000
	v_add_u32_e32 v0, s2, v155
	s_add_i32 s72, 0, 0x1c000
	ds_read_b128 v[138:141], v0
	ds_read_b128 v[142:145], v0 offset:1024
	ds_read_b128 v[162:165], v0 offset:2048
	ds_read_b128 v[180:183], v0 offset:3072
	v_add_u32_e32 v0, s72, v155
	ds_read_b128 v[188:191], v0
	ds_read_b128 v[192:195], v0 offset:1024
	ds_read_b128 v[196:199], v0 offset:2048
	ds_read_b128 v[200:203], v0 offset:3072
	s_mov_b32 m0, s67
	v_lshl_add_u64 v[136:137], s[70:71], 0, v[136:137]
	ds_read_b128 v[204:207], v184 offset:32768
	ds_read_b128 v[208:211], v184 offset:33792
	ds_read_b128 v[212:215], v184 offset:34816
	ds_read_b128 v[216:219], v184 offset:35840
	ds_read_b128 v[220:223], v184 offset:36864
	ds_read_b128 v[224:227], v184 offset:37888
	ds_read_b128 v[230:233], v184 offset:38912
	ds_read_b128 v[236:239], v184 offset:39936
	global_load_lds_dwordx4 v[136:137], off
	v_lshl_add_u64 v[134:135], s[70:71], 0, v[134:135]
	s_mov_b32 m0, s56
	s_nop 0
	global_load_lds_dwordx4 v[134:135], off
	s_waitcnt vmcnt(8)
	s_waitcnt lgkmcnt(0)
	s_barrier
	s_setprio 1
	s_waitcnt lgkmcnt(0)
	v_mfma_f32_16x16x32_bf16 v[122:125], v[138:141], v[204:207], v[122:125]
	v_mfma_f32_16x16x32_bf16 v[114:117], v[162:165], v[204:207], v[114:117]
	v_mfma_f32_16x16x32_bf16 v[106:109], v[138:141], v[212:215], v[106:109]
	v_mfma_f32_16x16x32_bf16 v[98:101], v[162:165], v[212:215], v[98:101]
	v_mfma_f32_16x16x32_bf16 v[94:97], v[138:141], v[220:223], v[94:97]
	v_mfma_f32_16x16x32_bf16 v[90:93], v[162:165], v[220:223], v[90:93]
	v_mfma_f32_16x16x32_bf16 v[86:89], v[138:141], v[230:233], v[86:89]
	v_mfma_f32_16x16x32_bf16 v[82:85], v[162:165], v[230:233], v[82:85]
	v_mfma_f32_16x16x32_bf16 v[122:125], v[142:145], v[208:211], v[122:125]
	v_mfma_f32_16x16x32_bf16 v[114:117], v[180:183], v[208:211], v[114:117]
	v_mfma_f32_16x16x32_bf16 v[106:109], v[142:145], v[216:219], v[106:109]
	v_mfma_f32_16x16x32_bf16 v[98:101], v[180:183], v[216:219], v[98:101]
	v_mfma_f32_16x16x32_bf16 v[94:97], v[142:145], v[224:227], v[94:97]
	v_mfma_f32_16x16x32_bf16 v[90:93], v[180:183], v[224:227], v[90:93]
	v_mfma_f32_16x16x32_bf16 v[86:89], v[142:145], v[236:239], v[86:89]
	v_mfma_f32_16x16x32_bf16 v[82:85], v[180:183], v[236:239], v[82:85]
	s_setprio 0
	s_setprio 1
	v_mfma_f32_16x16x32_bf16 v[78:81], v[188:191], v[204:207], v[78:81]
	v_mfma_f32_16x16x32_bf16 v[74:77], v[196:199], v[204:207], v[74:77]
	v_mfma_f32_16x16x32_bf16 v[70:73], v[188:191], v[212:215], v[70:73]
	v_mfma_f32_16x16x32_bf16 v[66:69], v[196:199], v[212:215], v[66:69]
	v_mfma_f32_16x16x32_bf16 v[62:65], v[188:191], v[220:223], v[62:65]
	v_mfma_f32_16x16x32_bf16 v[58:61], v[196:199], v[220:223], v[58:61]
	v_mfma_f32_16x16x32_bf16 v[54:57], v[188:191], v[230:233], v[54:57]
	v_mfma_f32_16x16x32_bf16 v[50:53], v[196:199], v[230:233], v[50:53]
	v_mfma_f32_16x16x32_bf16 v[78:81], v[192:195], v[208:211], v[78:81]
	v_mfma_f32_16x16x32_bf16 v[74:77], v[200:203], v[208:211], v[74:77]
	v_mfma_f32_16x16x32_bf16 v[70:73], v[192:195], v[216:219], v[70:73]
	v_mfma_f32_16x16x32_bf16 v[66:69], v[200:203], v[216:219], v[66:69]
	v_mfma_f32_16x16x32_bf16 v[62:65], v[192:195], v[224:227], v[62:65]
	v_mfma_f32_16x16x32_bf16 v[58:61], v[200:203], v[224:227], v[58:61]
	v_mfma_f32_16x16x32_bf16 v[54:57], v[192:195], v[236:239], v[54:57]
	v_mfma_f32_16x16x32_bf16 v[50:53], v[200:203], v[236:239], v[50:53]
	s_setprio 0
	s_barrier
; #define PG8_STAGE(bufoff, gbase, voff) do { _Pragma("unroll") for (int _i = 0; _i < 2; ++_i) \
;         __builtin_amdgcn_global_load_lds((const unsigned*)((const char*)(gbase) + (voff)[_i]), (PG8_LAS unsigned*)(lds + (bufoff) + ldsw + _i * 8192), 16, 0, 0); } while (0)
; #define PG8_LDA(dst, b, h) do { _Pragma("unroll") for (int m = 0; m < 4; ++m) _Pragma("unroll") for (int k = 0; k < 2; ++k) dst[m][k] = *(const PG8_LAS bf16x8*)(lds + PG8_SA(b, h) + aoff + m * 2048 + k * 1024); } while (0)
; #define PG8_MMA(ai, bj, At, Bt) do { __builtin_amdgcn_s_setprio(1); _Pragma("unroll") for (int m = 0; m < 4; ++m) _Pragma("unroll") for (int n = 0; n < 2; ++n) _Pragma("unroll") for (int k = 0; k < 2; ++k) \
;         acc[ai][bj][m][n] = __builtin_amdgcn_mfma_f32_16x16x32_bf16(Bt[n][k], At[m][k], acc[ai][bj][m][n], 0, 0, 0); __builtin_amdgcn_s_setprio(0); } while (0)
; #define PG8_WAIT_V(n) asm volatile("s_waitcnt vmcnt(" #n ")" ::: "memory")
; #define PG8_WAIT_L(n) asm volatile("s_waitcnt lgkmcnt(" #n ")" ::: "memory")
; #define PG8_BAR __builtin_amdgcn_s_barrier()
; #define PG8_SCHED __builtin_amdgcn_sched_barrier(0)
; template <class Epi, class Sched, bool ALIGN_EPI = false, bool SP2 = false, bool GATHER = false>
; __device__ __forceinline__ void gemm_phase(PG8_LAS unsigned char* lds, const Gemm g, const Sched& S, const Epi& E, const int2* gslot = nullptr, PG8_LAS unsigned char* gtab = nullptr) {
;     ...
;             PG8_LDA(At, 1, 1); PG8_STAGE(PG8_SB(1, 0), b3, voffB); PG8_STAGE(PG8_SB(1, 1), b3 + hstep, voffB); PG8_STAGE(PG8_SA(1, 0), a3, PG8_VA(vS, 0));
;             PG8_WAIT_V(8); PG8_WAIT_L(0); PG8_BAR; PG8_MMA(1, 0, At, B0); PG8_MMA(1, 1, At, B1); PG8_BAR; PG8_SCHED;
	s_add_i32 s2, s2, s47
	v_lshl_add_u64 v[166:167], v[166:167], 0, s[54:55]
	s_mov_b32 m0, s2
	ds_read_b128 v[134:137], v184 offset:49152
	ds_read_b128 v[204:207], v184 offset:50176
	ds_read_b128 v[208:211], v184 offset:51200
	ds_read_b128 v[212:215], v184 offset:52224
	ds_read_b128 v[216:219], v184 offset:53248
	ds_read_b128 v[220:223], v184 offset:54272
	ds_read_b128 v[224:227], v184 offset:55296
	ds_read_b128 v[230:233], v184 offset:56320
	global_load_lds_dwordx4 v[166:167], off
	s_add_i32 m0, s2, 0x2000
	s_add_u32 s70, vcc_lo, 0x40080
	v_lshl_add_u64 v[166:167], v[244:245], 0, s[54:55]
	s_addc_u32 s71, vcc_hi, 0
	s_add_i32 s2, s72, s47
	global_load_lds_dwordx4 v[166:167], off
	v_lshl_add_u64 v[166:167], s[70:71], 0, v[148:149]
	s_mov_b32 m0, s2
	s_nop 0
	global_load_lds_dwordx4 v[166:167], off
	v_lshl_add_u64 v[166:167], s[70:71], 0, v[150:151]
	s_add_i32 m0, s2, 0x2000
	s_nop 0
	global_load_lds_dwordx4 v[166:167], off
	v_lshl_add_u64 v[166:167], v[246:247], 0, s[54:55]
	s_mov_b32 m0, s0
	s_nop 0
	global_load_lds_dwordx4 v[166:167], off
	v_lshl_add_u64 v[166:167], v[248:249], 0, s[54:55]
	s_mov_b32 m0, s43
	s_nop 0
	global_load_lds_dwordx4 v[166:167], off
	s_waitcnt vmcnt(6)
	s_waitcnt lgkmcnt(0)
	s_barrier
	s_setprio 1
	s_waitcnt lgkmcnt(0)
	v_mfma_f32_16x16x32_bf16 v[46:49], v[138:141], v[134:137], v[46:49]
	v_mfma_f32_16x16x32_bf16 v[42:45], v[162:165], v[134:137], v[42:45]
	v_mfma_f32_16x16x32_bf16 v[38:41], v[138:141], v[208:211], v[38:41]
	v_mfma_f32_16x16x32_bf16 v[34:37], v[162:165], v[208:211], v[34:37]
	v_mfma_f32_16x16x32_bf16 v[30:33], v[138:141], v[216:219], v[30:33]
	v_mfma_f32_16x16x32_bf16 v[26:29], v[162:165], v[216:219], v[26:29]
	v_mfma_f32_16x16x32_bf16 v[6:9], v[138:141], v[224:227], v[6:9]
	v_mfma_f32_16x16x32_bf16 v[2:5], v[162:165], v[224:227], v[2:5]
	v_mfma_f32_16x16x32_bf16 v[46:49], v[142:145], v[204:207], v[46:49]
	v_mfma_f32_16x16x32_bf16 v[42:45], v[180:183], v[204:207], v[42:45]
	v_mfma_f32_16x16x32_bf16 v[38:41], v[142:145], v[212:215], v[38:41]
	v_mfma_f32_16x16x32_bf16 v[34:37], v[180:183], v[212:215], v[34:37]
	v_mfma_f32_16x16x32_bf16 v[30:33], v[142:145], v[220:223], v[30:33]
	v_mfma_f32_16x16x32_bf16 v[26:29], v[180:183], v[220:223], v[26:29]
	v_mfma_f32_16x16x32_bf16 v[6:9], v[142:145], v[230:233], v[6:9]
	v_mfma_f32_16x16x32_bf16 v[2:5], v[180:183], v[230:233], v[2:5]
	s_setprio 0
	s_setprio 1
	v_mfma_f32_16x16x32_bf16 v[22:25], v[188:191], v[134:137], v[22:25]
	v_mfma_f32_16x16x32_bf16 v[18:21], v[196:199], v[134:137], v[18:21]
	v_mfma_f32_16x16x32_bf16 v[14:17], v[188:191], v[208:211], v[14:17]
	v_mfma_f32_16x16x32_bf16 v[10:13], v[196:199], v[208:211], v[10:13]
	v_mfma_f32_16x16x32_bf16 v[102:105], v[188:191], v[216:219], v[102:105]
	v_mfma_f32_16x16x32_bf16 v[110:113], v[196:199], v[216:219], v[110:113]
	v_mfma_f32_16x16x32_bf16 v[118:121], v[188:191], v[224:227], v[118:121]
	v_mfma_f32_16x16x32_bf16 v[126:129], v[196:199], v[224:227], v[126:129]
	v_mfma_f32_16x16x32_bf16 v[22:25], v[192:195], v[204:207], v[22:25]
	v_mfma_f32_16x16x32_bf16 v[18:21], v[200:203], v[204:207], v[18:21]
	v_mfma_f32_16x16x32_bf16 v[14:17], v[192:195], v[212:215], v[14:17]
	v_mfma_f32_16x16x32_bf16 v[10:13], v[200:203], v[212:215], v[10:13]
	v_mfma_f32_16x16x32_bf16 v[102:105], v[192:195], v[220:223], v[102:105]
	v_mfma_f32_16x16x32_bf16 v[110:113], v[200:203], v[220:223], v[110:113]
	v_mfma_f32_16x16x32_bf16 v[118:121], v[192:195], v[230:233], v[118:121]
	v_mfma_f32_16x16x32_bf16 v[126:129], v[200:203], v[230:233], v[126:129]
	s_setprio 0
	s_barrier
	s_add_i32 s69, s69, 2
	s_add_u32 s60, s60, 0x100
	s_addc_u32 s61, s61, 0
	s_cmp_gt_u32 s69, 13
	s_cbranch_scc1 .LBB0_1097
